# PEER V gather loop: first-half expert-row prefetch issued behind the drain (in flight during the batch's 64 MFMAs) with a counted vmcnt(16) before the second half uses it, instead of being drained rig
# speedup vs baseline: 1.0427x; 1.0035x over previous
; #define PL_LOAD(RB, TAB, SE, BB) do { _Pragma("unroll") for (int _q = 0; _q < 16; ++_q) { \
;         const unsigned _pw = (unsigned)__builtin_amdgcn_readlane((int)(SE), (BB) * 8 + (_q >> 1)); const unsigned _idx = (_q & 1) ? (_pw >> 16) : (_pw & 0xffffu); \
;         (RB)[_q] = *(const v4u*)((TAB) + (size_t)_idx * 1024 + 16 * lane); } } while (0)
; __device__ __forceinline__ void peer_unit(Frame& F, const Args& a, int layer, int unit, bool last) {
;     ...
;             if (lt < 16) PL_LOAD(rb, V8, seL, lb);
.LBB0_1787:
.LBB0_1789:
	s_cmp_lg_u32 s56, s52
	s_cbranch_scc1 .LBB0_1798
	s_ashr_i32 s30, s58, 31
	s_add_u32 s52, s0, s58
	s_addc_u32 s53, s1, s30
	s_lshl_b64 s[38:39], s[52:53], 12
	v_cndmask_b32_e64 v1, 0, 1, s[44:45]
	v_lshl_add_u64 v[2:3], v[232:233], 0, s[38:39]
	v_cmp_ne_u32_e64 s[38:39], 1, v1
	s_andn2_b64 vcc, exec, s[44:45]
	s_cbranch_vccnz .LBB0_1799
	global_load_dwordx4 v[128:131], v[2:3], off
	s_and_b64 vcc, exec, s[38:39]
	s_cbranch_vccz .LBB0_1800

.LBB0_1808:
	s_lshl_b32 s38, s58, 9
	s_add_i32 s38, s15, s38
	s_lshl_b32 s39, s56, 6
	s_add_i32 s38, s38, s39
	s_waitcnt vmcnt(0)
	v_mov_b32_e32 v168, s38
	ds_read_b128 v[170:173], v168
	s_cmp_gt_i32 s57, 15
	s_cbranch_scc1 .Lpv_skip1
	s_lshl_b32 s38, s59, 3
	s_waitcnt lgkmcnt(0)
	v_readlane_b32 s39, v250, s38
	s_lshl_b32 s30, s39, 10
	s_and_b32 s30, s30, 0x3fffc00
	v_lshl_add_u64 v[2:3], v[226:227], 0, s[30:31]
	s_bfe_u32 s30, s39, 0x100010
	s_lshl_b32 s30, s30, 10
	v_lshl_add_u64 v[8:9], v[226:227], 0, s[30:31]
	s_or_b32 s30, s38, 1
	v_readlane_b32 s39, v250, s30
	s_lshl_b32 s30, s39, 10
	s_and_b32 s30, s30, 0x3fffc00
	global_load_dwordx4 v[4:7], v[2:3], off
	s_nop 0
	global_load_dwordx4 v[8:11], v[8:9], off
	v_lshl_add_u64 v[2:3], v[226:227], 0, s[30:31]
	s_bfe_u32 s30, s39, 0x100010
	s_lshl_b32 s30, s30, 10
	v_lshl_add_u64 v[16:17], v[226:227], 0, s[30:31]
	s_or_b32 s30, s38, 2
	v_readlane_b32 s39, v250, s30
	s_lshl_b32 s30, s39, 10
	s_and_b32 s30, s30, 0x3fffc00
	global_load_dwordx4 v[12:15], v[2:3], off
	s_nop 0
	global_load_dwordx4 v[16:19], v[16:17], off
	v_lshl_add_u64 v[2:3], v[226:227], 0, s[30:31]
	s_bfe_u32 s30, s39, 0x100010
	s_lshl_b32 s30, s30, 10
	v_lshl_add_u64 v[24:25], v[226:227], 0, s[30:31]
	s_or_b32 s30, s38, 3
	v_readlane_b32 s39, v250, s30
	s_lshl_b32 s30, s39, 10
	s_and_b32 s30, s30, 0x3fffc00
	global_load_dwordx4 v[20:23], v[2:3], off
	s_nop 0
	global_load_dwordx4 v[24:27], v[24:25], off
	v_lshl_add_u64 v[2:3], v[226:227], 0, s[30:31]
	s_bfe_u32 s30, s39, 0x100010
	s_lshl_b32 s30, s30, 10
	v_lshl_add_u64 v[32:33], v[226:227], 0, s[30:31]
	s_or_b32 s30, s38, 4
	v_readlane_b32 s39, v250, s30
	s_lshl_b32 s30, s39, 10
	s_and_b32 s30, s30, 0x3fffc00
	global_load_dwordx4 v[28:31], v[2:3], off
	s_nop 0
	global_load_dwordx4 v[32:35], v[32:33], off
	v_lshl_add_u64 v[2:3], v[226:227], 0, s[30:31]
	s_bfe_u32 s30, s39, 0x100010
	s_lshl_b32 s30, s30, 10
	v_lshl_add_u64 v[40:41], v[226:227], 0, s[30:31]
	s_or_b32 s30, s38, 5
	v_readlane_b32 s39, v250, s30
	s_lshl_b32 s30, s39, 10
	s_and_b32 s30, s30, 0x3fffc00
	global_load_dwordx4 v[36:39], v[2:3], off
	s_nop 0
	global_load_dwordx4 v[40:43], v[40:41], off
	v_lshl_add_u64 v[2:3], v[226:227], 0, s[30:31]
	s_bfe_u32 s30, s39, 0x100010
	s_lshl_b32 s30, s30, 10
	v_lshl_add_u64 v[48:49], v[226:227], 0, s[30:31]
	s_or_b32 s30, s38, 6
	v_readlane_b32 s39, v250, s30
	s_lshl_b32 s30, s39, 10
	s_and_b32 s30, s30, 0x3fffc00
	global_load_dwordx4 v[44:47], v[2:3], off
	s_nop 0
	global_load_dwordx4 v[48:51], v[48:49], off
	v_lshl_add_u64 v[2:3], v[226:227], 0, s[30:31]
	s_bfe_u32 s30, s39, 0x100010
	s_lshl_b32 s30, s30, 10
	v_lshl_add_u64 v[56:57], v[226:227], 0, s[30:31]
	s_or_b32 s30, s38, 7
	v_readlane_b32 s38, v250, s30
	s_lshl_b32 s30, s38, 10
	s_and_b32 s30, s30, 0x3fffc00
	global_load_dwordx4 v[52:55], v[2:3], off
	s_nop 0
	global_load_dwordx4 v[56:59], v[56:57], off
	v_lshl_add_u64 v[2:3], v[226:227], 0, s[30:31]
	s_bfe_u32 s30, s38, 0x100010
	s_lshl_b32 s30, s30, 10
	v_lshl_add_u64 v[64:65], v[226:227], 0, s[30:31]
	global_load_dwordx4 v[60:63], v[2:3], off
	s_nop 0
	global_load_dwordx4 v[64:67], v[64:65], off
.Lpv_skip1:
	s_lshl_b32 s30, s56, 4
	s_cmp_ge_i32 s30, s60
	s_cselect_b64 s[38:39], -1, 0
	s_cmp_lt_i32 s30, s48
	s_cselect_b64 s[52:53], -1, 0
	s_waitcnt lgkmcnt(0)
	v_mul_f32_e32 v1, 0x45000000, v170
	s_and_b64 vcc, s[38:39], s[52:53]
	v_cndmask_b32_e32 v1, 0, v1, vcc
	v_mov_b32_e32 v2, v0
	s_or_b32 s52, s30, 1
	v_cvt_pk_fp8_f32 v2, v1, v1
	s_cmp_ge_i32 s52, s60
	s_cselect_b64 s[38:39], -1, 0
	s_cmp_lt_i32 s52, s48
	s_cselect_b64 s[52:53], -1, 0
	v_mul_f32_e32 v169, 0x45000000, v171
	s_and_b64 vcc, s[38:39], s[52:53]
	v_cvt_pk_fp8_f32 v2, v1, v1 op_sel:[0,0,1]
	v_cndmask_b32_e32 v169, 0, v169, vcc
	v_mov_b32_e32 v170, v0
	v_cvt_pk_fp8_f32 v170, v169, v169
	v_mov_b32_e32 v3, v0
	v_and_b32_e32 v2, v2, v249
	s_or_b32 s52, s30, 2
	v_cvt_pk_fp8_f32 v170, v169, v169 op_sel:[0,0,1]
	s_cmp_ge_i32 s52, s60
	s_cselect_b64 s[38:39], -1, 0
	s_cmp_lt_i32 s52, s48
	s_cselect_b64 s[52:53], -1, 0
	v_mul_f32_e32 v169, 0x45000000, v172
	s_and_b64 vcc, s[38:39], s[52:53]
	v_mov_b32_e32 v1, v2
	s_nop 0
	v_mfma_f32_16x16x32_fp8_fp8 v[160:163], v[2:3], v[68:69], v[160:163]
	v_cndmask_b32_e32 v169, 0, v169, vcc
	s_or_b32 s52, s30, 3
	s_cmp_ge_i32 s52, s60
	v_mfma_f32_16x16x32_fp8_fp8 v[152:155], v[2:3], v[70:71], v[152:155]
	v_and_b32_e32 v2, v170, v249
	v_mov_b32_e32 v170, v0
	v_cvt_pk_fp8_f32 v170, v169, v169
	v_mfma_f32_16x16x32_fp8_fp8 v[164:167], v[0:1], v[68:69], v[164:167]
	s_cselect_b64 s[38:39], -1, 0
	s_cmp_lt_i32 s52, s48
	v_cvt_pk_fp8_f32 v170, v169, v169 op_sel:[0,0,1]
	v_mfma_f32_16x16x32_fp8_fp8 v[156:159], v[0:1], v[70:71], v[156:159]
	v_mov_b32_e32 v1, v2
	s_cselect_b64 s[52:53], -1, 0
	s_and_b64 vcc, s[38:39], s[52:53]
	s_nop 0
	v_mfma_f32_16x16x32_fp8_fp8 v[160:163], v[2:3], v[72:73], v[160:163]
	s_or_b32 s52, s30, 4
	s_cmp_ge_i32 s52, s60
	s_cselect_b64 s[38:39], -1, 0
	v_mfma_f32_16x16x32_fp8_fp8 v[152:155], v[2:3], v[74:75], v[152:155]
	v_and_b32_e32 v2, v170, v249
	v_mov_b32_e32 v170, v0
	s_cmp_lt_i32 s52, s48
	s_nop 0
	v_mfma_f32_16x16x32_fp8_fp8 v[184:187], v[2:3], v[76:77], v[160:163]
	s_cselect_b64 s[52:53], -1, 0
	s_nop 1
	v_mul_f32_e32 v160, 0x45000000, v173
	v_cndmask_b32_e32 v169, 0, v160, vcc
	v_cvt_pk_fp8_f32 v170, v169, v169
	v_mfma_f32_16x16x32_fp8_fp8 v[164:167], v[0:1], v[72:73], v[164:167]
	s_and_b64 vcc, s[38:39], s[52:53]
	s_or_b32 s52, s30, 5
	v_cvt_pk_fp8_f32 v170, v169, v169 op_sel:[0,0,1]
	v_mfma_f32_16x16x32_fp8_fp8 v[156:159], v[0:1], v[74:75], v[156:159]
	v_mov_b32_e32 v1, v2
	s_cmp_ge_i32 s52, s60
	s_cselect_b64 s[38:39], -1, 0
	v_mfma_f32_16x16x32_fp8_fp8 v[160:163], v[2:3], v[78:79], v[152:155]
	v_and_b32_e32 v2, v170, v249
	ds_read_b128 v[170:173], v168 offset:16
	s_cmp_lt_i32 s52, s48
	s_cselect_b64 s[52:53], -1, 0
	v_mfma_f32_16x16x32_fp8_fp8 v[164:167], v[0:1], v[76:77], v[164:167]
	s_waitcnt lgkmcnt(0)
	v_mul_f32_e32 v169, 0x45000000, v170
	v_cndmask_b32_e32 v169, 0, v169, vcc
	v_mov_b32_e32 v170, v0
	v_cvt_pk_fp8_f32 v170, v169, v169
	s_and_b64 vcc, s[38:39], s[52:53]
	v_mfma_f32_16x16x32_fp8_fp8 v[156:159], v[0:1], v[78:79], v[156:159]
	v_mov_b32_e32 v1, v2
	v_cvt_pk_fp8_f32 v170, v169, v169 op_sel:[0,0,1]
	v_mul_f32_e32 v169, 0x45000000, v171
	s_nop 0
	v_mfma_f32_16x16x32_fp8_fp8 v[152:155], v[2:3], v[80:81], v[184:187]
	v_cndmask_b32_e32 v169, 0, v169, vcc
	s_or_b32 s52, s30, 6
	s_cmp_ge_i32 s52, s60
	v_mfma_f32_16x16x32_fp8_fp8 v[160:163], v[2:3], v[82:83], v[160:163]
	v_and_b32_e32 v2, v170, v249
	v_mov_b32_e32 v170, v0
	v_cvt_pk_fp8_f32 v170, v169, v169
	s_cselect_b64 s[38:39], -1, 0
	s_cmp_lt_i32 s52, s48
	s_cselect_b64 s[52:53], -1, 0
	v_cvt_pk_fp8_f32 v170, v169, v169 op_sel:[0,0,1]
	v_mul_f32_e32 v169, 0x45000000, v172
	s_and_b64 vcc, s[38:39], s[52:53]
	v_mfma_f32_16x16x32_fp8_fp8 v[164:167], v[0:1], v[80:81], v[164:167]
	v_cndmask_b32_e32 v169, 0, v169, vcc
	s_or_b32 s52, s30, 7
	s_cmp_ge_i32 s52, s60
	v_mfma_f32_16x16x32_fp8_fp8 v[156:159], v[0:1], v[82:83], v[156:159]
	v_mov_b32_e32 v1, v2
	s_cselect_b64 s[38:39], -1, 0
	s_cmp_lt_i32 s52, s48
	s_nop 0
	v_mfma_f32_16x16x32_fp8_fp8 v[152:155], v[2:3], v[84:85], v[152:155]
	s_cselect_b64 s[52:53], -1, 0
	s_and_b64 vcc, s[38:39], s[52:53]
	s_or_b32 s52, s30, 8
	v_mfma_f32_16x16x32_fp8_fp8 v[160:163], v[2:3], v[86:87], v[160:163]
	v_and_b32_e32 v2, v170, v249
	v_mov_b32_e32 v170, v0
	v_cvt_pk_fp8_f32 v170, v169, v169
	v_mfma_f32_16x16x32_fp8_fp8 v[164:167], v[0:1], v[84:85], v[164:167]
	s_cmp_ge_i32 s52, s60
	s_cselect_b64 s[38:39], -1, 0
	v_cvt_pk_fp8_f32 v170, v169, v169 op_sel:[0,0,1]
	v_mul_f32_e32 v169, 0x45000000, v173
	v_mfma_f32_16x16x32_fp8_fp8 v[156:159], v[0:1], v[86:87], v[156:159]
	v_mov_b32_e32 v1, v2
	v_cndmask_b32_e32 v169, 0, v169, vcc
	s_cmp_lt_i32 s52, s48
	s_nop 0
	v_mfma_f32_16x16x32_fp8_fp8 v[152:155], v[2:3], v[88:89], v[152:155]
	s_cselect_b64 s[52:53], -1, 0
	s_and_b64 vcc, s[38:39], s[52:53]
	s_or_b32 s52, s30, 9
	v_mfma_f32_16x16x32_fp8_fp8 v[160:163], v[2:3], v[90:91], v[160:163]
	v_and_b32_e32 v2, v170, v249
	v_mov_b32_e32 v170, v0
	v_cvt_pk_fp8_f32 v170, v169, v169
	v_mfma_f32_16x16x32_fp8_fp8 v[164:167], v[0:1], v[88:89], v[164:167]
	s_cmp_ge_i32 s52, s60
	s_cselect_b64 s[38:39], -1, 0
	v_cvt_pk_fp8_f32 v170, v169, v169 op_sel:[0,0,1]
	v_mfma_f32_16x16x32_fp8_fp8 v[156:159], v[0:1], v[90:91], v[156:159]
	v_mov_b32_e32 v1, v2
	s_cmp_lt_i32 s52, s48
	s_cselect_b64 s[52:53], -1, 0
	s_nop 0
	v_mfma_f32_16x16x32_fp8_fp8 v[152:155], v[2:3], v[92:93], v[152:155]
	v_mfma_f32_16x16x32_fp8_fp8 v[160:163], v[2:3], v[94:95], v[160:163]
	v_and_b32_e32 v2, v170, v249
	ds_read_b128 v[170:173], v168 offset:32
	s_waitcnt lgkmcnt(0)
	v_mul_f32_e32 v169, 0x45000000, v170
	v_cndmask_b32_e32 v169, 0, v169, vcc
	v_mov_b32_e32 v170, v0
	v_cvt_pk_fp8_f32 v170, v169, v169
	s_and_b64 vcc, s[38:39], s[52:53]
	v_mfma_f32_16x16x32_fp8_fp8 v[164:167], v[0:1], v[92:93], v[164:167]
	s_or_b32 s52, s30, 10
	v_cvt_pk_fp8_f32 v170, v169, v169 op_sel:[0,0,1]
	v_mul_f32_e32 v169, 0x45000000, v171
	v_mfma_f32_16x16x32_fp8_fp8 v[156:159], v[0:1], v[94:95], v[156:159]
	v_mov_b32_e32 v1, v2
	v_cndmask_b32_e32 v169, 0, v169, vcc
	s_cmp_ge_i32 s52, s60
	s_nop 0
	v_mfma_f32_16x16x32_fp8_fp8 v[152:155], v[2:3], v[96:97], v[152:155]
	s_cselect_b64 s[38:39], -1, 0
	s_cmp_lt_i32 s52, s48
	s_cselect_b64 s[52:53], -1, 0
	v_mfma_f32_16x16x32_fp8_fp8 v[160:163], v[2:3], v[98:99], v[160:163]
	v_and_b32_e32 v2, v170, v249
	v_mov_b32_e32 v170, v0
	v_cvt_pk_fp8_f32 v170, v169, v169
	s_and_b64 vcc, s[38:39], s[52:53]
	v_mfma_f32_16x16x32_fp8_fp8 v[164:167], v[0:1], v[96:97], v[164:167]
	s_or_b32 s52, s30, 11
	v_cvt_pk_fp8_f32 v170, v169, v169 op_sel:[0,0,1]
	v_mul_f32_e32 v169, 0x45000000, v172
	v_mfma_f32_16x16x32_fp8_fp8 v[156:159], v[0:1], v[98:99], v[156:159]
	v_mov_b32_e32 v1, v2
	v_cndmask_b32_e32 v169, 0, v169, vcc
	s_cmp_ge_i32 s52, s60
	s_nop 0
	v_mfma_f32_16x16x32_fp8_fp8 v[152:155], v[2:3], v[100:101], v[152:155]
	s_cselect_b64 s[38:39], -1, 0
	s_cmp_lt_i32 s52, s48
	s_cselect_b64 s[52:53], -1, 0
	v_mfma_f32_16x16x32_fp8_fp8 v[160:163], v[2:3], v[102:103], v[160:163]
	v_and_b32_e32 v2, v170, v249
	v_mov_b32_e32 v170, v0
	v_cvt_pk_fp8_f32 v170, v169, v169
	s_and_b64 vcc, s[38:39], s[52:53]
	v_mfma_f32_16x16x32_fp8_fp8 v[164:167], v[0:1], v[100:101], v[164:167]
	s_or_b32 s52, s30, 12
	v_cvt_pk_fp8_f32 v170, v169, v169 op_sel:[0,0,1]
	v_mul_f32_e32 v169, 0x45000000, v173
	v_mfma_f32_16x16x32_fp8_fp8 v[156:159], v[0:1], v[102:103], v[156:159]
	v_mov_b32_e32 v1, v2
	v_cndmask_b32_e32 v169, 0, v169, vcc
	s_cmp_ge_i32 s52, s60
	s_nop 0
	v_mfma_f32_16x16x32_fp8_fp8 v[152:155], v[2:3], v[104:105], v[152:155]
	s_cselect_b64 s[38:39], -1, 0
	s_cmp_lt_i32 s52, s48
	s_cselect_b64 s[52:53], -1, 0
	v_mfma_f32_16x16x32_fp8_fp8 v[160:163], v[2:3], v[106:107], v[160:163]
	v_and_b32_e32 v2, v170, v249
	v_mov_b32_e32 v170, v0
	v_cvt_pk_fp8_f32 v170, v169, v169
	v_mfma_f32_16x16x32_fp8_fp8 v[164:167], v[0:1], v[104:105], v[164:167]
	s_and_b64 vcc, s[38:39], s[52:53]
	v_mov_b32_e32 v172, v0
	v_cvt_pk_fp8_f32 v170, v169, v169 op_sel:[0,0,1]
	v_mfma_f32_16x16x32_fp8_fp8 v[156:159], v[0:1], v[106:107], v[156:159]
	v_mov_b32_e32 v1, v2
	s_or_b32 s52, s30, 13
	s_cmp_ge_i32 s52, s60
	s_nop 0
	v_mfma_f32_16x16x32_fp8_fp8 v[152:155], v[2:3], v[108:109], v[152:155]
	s_cselect_b64 s[38:39], -1, 0
	s_cmp_lt_i32 s52, s48
	s_cselect_b64 s[52:53], -1, 0
	v_mfma_f32_16x16x32_fp8_fp8 v[160:163], v[2:3], v[110:111], v[160:163]
	v_and_b32_e32 v2, v170, v249
	ds_read_b128 v[168:171], v168 offset:48
	v_mov_b32_e32 v173, v0
	v_mfma_f32_16x16x32_fp8_fp8 v[164:167], v[0:1], v[108:109], v[164:167]
	s_waitcnt lgkmcnt(0)
; __device__ __forceinline__ void peer_token_end(Frame& F, const Args& a, int layer, bool last, bool final_half, size_t tok, int lane, const f32x2 (&out)[8], const f32x4 (&hpre)[4], const v4u (&gpre)[2], const v4u& p8pre) {
;     ...
;     for (int i = 0; i < 4; ++i) { const f32x2 lo = __builtin_amdgcn_cvt_pk_f32_fp8((int)p8pre[i], false), hi = __builtin_amdgcn_cvt_pk_f32_fp8((int)p8pre[i], true);
;         pe[i] = (f32x4){lo.x, lo.y, hi.x, hi.y} * (1.f / 256.f) + (f32x4){out[2 * i].x, out[2 * i].y, out[2 * i + 1].x, out[2 * i + 1].y}; }
;     if (!final_half) {
;         v4u w;
; #pragma unroll
;         for (int i = 0; i < 4; ++i) { const f32x4 s8 = pe[i] * 256.f; int t = 0; t = __builtin_amdgcn_cvt_pk_fp8_f32(s8.x, s8.y, t, false); t = __builtin_amdgcn_cvt_pk_fp8_f32(s8.z, s8.w, t, true); w[i] = (unsigned)t; }
;         *(v4u*)((unsigned char*)(F.ws + WS_P8) + tok * 1024 + 16 * lane) = w;
	v_mul_f32_e32 v168, 0x45000000, v168
	v_cndmask_b32_e32 v168, 0, v168, vcc
	v_cvt_pk_fp8_f32 v172, v168, v168
	s_and_b64 vcc, s[38:39], s[52:53]
	v_mfma_f32_16x16x32_fp8_fp8 v[156:159], v[0:1], v[110:111], v[156:159]
	v_mov_b32_e32 v1, v2
	v_cvt_pk_fp8_f32 v172, v168, v168 op_sel:[0,0,1]
	v_mul_f32_e32 v168, 0x45000000, v169
	v_cndmask_b32_e32 v168, 0, v168, vcc
	v_mov_b32_e32 v169, v0
	v_cvt_pk_fp8_f32 v169, v168, v168
	s_nop 0
	v_mfma_f32_16x16x32_fp8_fp8 v[152:155], v[2:3], v[112:113], v[152:155]
	s_or_b32 s52, s30, 14
	s_cmp_ge_i32 s52, s60
	v_cvt_pk_fp8_f32 v169, v168, v168 op_sel:[0,0,1]
	v_mfma_f32_16x16x32_fp8_fp8 v[160:163], v[2:3], v[114:115], v[160:163]
	v_and_b32_e32 v2, v172, v249
	s_cselect_b64 s[38:39], -1, 0
	s_cmp_lt_i32 s52, s48
	s_cselect_b64 s[52:53], -1, 0
	v_mul_f32_e32 v168, 0x45000000, v170
	s_and_b64 vcc, s[38:39], s[52:53]
	v_mfma_f32_16x16x32_fp8_fp8 v[164:167], v[0:1], v[112:113], v[164:167]
	v_cndmask_b32_e32 v168, 0, v168, vcc
	s_or_b32 s30, s30, 15
	s_cmp_ge_i32 s30, s60
	v_mfma_f32_16x16x32_fp8_fp8 v[156:159], v[0:1], v[114:115], v[156:159]
	v_mov_b32_e32 v1, v2
	s_cselect_b64 s[38:39], -1, 0
	s_cmp_lt_i32 s30, s48
	s_nop 0
	v_mfma_f32_16x16x32_fp8_fp8 v[152:155], v[2:3], v[120:121], v[152:155]
	s_cselect_b64 s[52:53], -1, 0
	s_and_b64 vcc, s[38:39], s[52:53]
	s_add_i32 s30, s61, -1
	v_mfma_f32_16x16x32_fp8_fp8 v[160:163], v[2:3], v[122:123], v[160:163]
	v_and_b32_e32 v2, v169, v249
	v_mov_b32_e32 v169, v0
	v_cvt_pk_fp8_f32 v169, v168, v168
	v_mfma_f32_16x16x32_fp8_fp8 v[164:167], v[0:1], v[120:121], v[164:167]
	s_cmp_lg_u32 s56, s30
	v_cvt_pk_fp8_f32 v169, v168, v168 op_sel:[0,0,1]
	v_mul_f32_e32 v168, 0x45000000, v171
	v_mfma_f32_16x16x32_fp8_fp8 v[156:159], v[0:1], v[122:123], v[156:159]
	v_mov_b32_e32 v1, v2
	v_cndmask_b32_e32 v172, 0, v168, vcc
	v_cvt_pk_fp8_f32 v173, v172, v172
	s_nop 0
	v_mfma_f32_16x16x32_fp8_fp8 v[152:155], v[2:3], v[124:125], v[152:155]
	v_cvt_pk_fp8_f32 v173, v172, v172 op_sel:[0,0,1]
	v_mfma_f32_16x16x32_fp8_fp8 v[160:163], v[2:3], v[126:127], v[160:163]
	v_and_b32_e32 v2, v169, v249
	v_mfma_f32_16x16x32_fp8_fp8 v[164:167], v[0:1], v[124:125], v[164:167]
	v_mfma_f32_16x16x32_fp8_fp8 v[156:159], v[0:1], v[126:127], v[156:159]
	v_mov_b32_e32 v1, v2
	s_nop 0
	v_mfma_f32_16x16x32_fp8_fp8 v[152:155], v[2:3], v[144:145], v[152:155]
	v_mfma_f32_16x16x32_fp8_fp8 v[168:171], v[2:3], v[146:147], v[160:163]
	v_and_b32_e32 v2, v173, v249
	v_mfma_f32_16x16x32_fp8_fp8 v[164:167], v[0:1], v[144:145], v[164:167]
	v_mfma_f32_16x16x32_fp8_fp8 v[156:159], v[0:1], v[146:147], v[156:159]
	v_mov_b32_e32 v1, v2
	s_nop 0
	v_mfma_f32_16x16x32_fp8_fp8 v[160:163], v[2:3], v[148:149], v[152:155]
	v_mfma_f32_16x16x32_fp8_fp8 v[164:167], v[0:1], v[148:149], v[164:167]
	v_mfma_f32_16x16x32_fp8_fp8 v[152:155], v[2:3], v[150:151], v[168:171]
	v_mfma_f32_16x16x32_fp8_fp8 v[156:159], v[0:1], v[150:151], v[156:159]
	s_cbranch_scc1 .LBB0_1816
	v_cvt_pk_f32_fp8_e32 v[2:3], v140
	v_cvt_pk_f32_fp8_e32 v[170:171], v141
	v_cvt_pk_f32_fp8_sdwa v[172:173], v141 src0_sel:WORD_1
	v_cvt_pk_f32_fp8_sdwa v[188:189], v142 src0_sel:WORD_1
	v_pk_mul_f32 v[2:3], v[2:3], s[12:13] op_sel_hi:[1,0]
	v_cvt_pk_f32_fp8_e32 v[186:187], v142
	v_pk_fma_f32 v[174:175], v[160:161], s[14:15], v[2:3] op_sel_hi:[1,0,1]
	v_pk_mul_f32 v[2:3], v[170:171], s[12:13] op_sel_hi:[1,0]
	v_pk_mul_f32 v[170:171], v[172:173], s[12:13] op_sel_hi:[1,0]
	v_cvt_pk_f32_fp8_sdwa v[168:169], v140 src0_sel:WORD_1
	v_pk_fma_f32 v[172:173], v[166:167], s[14:15], v[170:171] op_sel_hi:[1,0,1]
	v_pk_mul_f32 v[170:171], v[188:189], s[12:13] op_sel_hi:[1,0]
	v_cvt_pk_f32_fp8_e32 v[188:189], v143
	v_cvt_pk_f32_fp8_sdwa v[192:193], v143 src0_sel:WORD_1
	s_ashr_i32 s30, s58, 31
	s_add_u32 s52, s0, s58
	v_pk_fma_f32 v[184:185], v[164:165], s[14:15], v[2:3] op_sel_hi:[1,0,1]
	v_pk_mul_f32 v[2:3], v[186:187], s[12:13] op_sel_hi:[1,0]
	s_addc_u32 s53, s1, s30
	v_pk_mul_f32 v[168:169], v[168:169], s[12:13] op_sel_hi:[1,0]
	v_pk_fma_f32 v[186:187], v[154:155], s[14:15], v[170:171] op_sel_hi:[1,0,1]
	v_pk_fma_f32 v[190:191], v[152:153], s[14:15], v[2:3] op_sel_hi:[1,0,1]
	v_pk_mul_f32 v[2:3], v[188:189], s[12:13] op_sel_hi:[1,0]
	v_pk_mul_f32 v[170:171], v[192:193], s[12:13] op_sel_hi:[1,0]
	s_lshl_b64 s[38:39], s[52:53], 10
	v_pk_fma_f32 v[168:169], v[162:163], s[14:15], v[168:169] op_sel_hi:[1,0,1]
	v_pk_fma_f32 v[188:189], v[158:159], s[14:15], v[170:171] op_sel_hi:[1,0,1]
	v_pk_fma_f32 v[192:193], v[156:157], s[14:15], v[2:3] op_sel_hi:[1,0,1]
	s_andn2_b64 vcc, exec, s[46:47]
	s_mov_b64 s[54:55], -1
	s_cbranch_vccnz .LBB0_1811
	v_pk_mul_f32 v[2:3], v[174:175], s[8:9] op_sel_hi:[1,0]
	v_mov_b32_e32 v194, v0
	v_cvt_pk_fp8_f32 v194, v2, v3
	v_pk_mul_f32 v[2:3], v[184:185], s[8:9] op_sel_hi:[1,0]
	v_mov_b32_e32 v195, v0
	v_cvt_pk_fp8_f32 v195, v2, v3
	v_pk_mul_f32 v[2:3], v[168:169], s[8:9] op_sel_hi:[1,0]
	v_mov_b32_e32 v196, v0
	v_cvt_pk_fp8_f32 v194, v2, v3 op_sel:[0,0,1]
	v_pk_mul_f32 v[2:3], v[172:173], s[8:9] op_sel_hi:[1,0]
	v_mov_b32_e32 v197, v0
	v_cvt_pk_fp8_f32 v195, v2, v3 op_sel:[0,0,1]
	v_pk_mul_f32 v[2:3], v[190:191], s[8:9] op_sel_hi:[1,0]
	s_mov_b64 s[54:55], 0
	v_cvt_pk_fp8_f32 v196, v2, v3
	v_pk_mul_f32 v[2:3], v[192:193], s[8:9] op_sel_hi:[1,0]
	s_nop 0
	v_cvt_pk_fp8_f32 v197, v2, v3
	v_pk_mul_f32 v[2:3], v[186:187], s[8:9] op_sel_hi:[1,0]
	s_nop 0
	v_cvt_pk_fp8_f32 v196, v2, v3 op_sel:[0,0,1]
	v_pk_mul_f32 v[2:3], v[188:189], s[8:9] op_sel_hi:[1,0]
	s_nop 0
	v_cvt_pk_fp8_f32 v197, v2, v3 op_sel:[0,0,1]
	v_lshl_add_u64 v[2:3], v[234:235], 0, s[38:39]
	global_store_dwordx4 v[2:3], v[194:197], off

; #define PL_LOAD(RB, TAB, SE, BB) do { _Pragma("unroll") for (int _q = 0; _q < 16; ++_q) { \
;         const unsigned _pw = (unsigned)__builtin_amdgcn_readlane((int)(SE), (BB) * 8 + (_q >> 1)); const unsigned _idx = (_q & 1) ? (_pw >> 16) : (_pw & 0xffffu); \
;         (RB)[_q] = *(const v4u*)((TAB) + (size_t)_idx * 1024 + 16 * lane); } } while (0)
; __device__ __forceinline__ void peer_unit(Frame& F, const Args& a, int layer, int unit, bool last) {
;     ...
;             if (lt < 16) PL_LOAD(ra, V8, seL, lb);
.LBB0_1821:
	s_cmp_gt_i32 s58, 15
	s_cbranch_scc1 .LBB0_1823
	s_lshl_b32 s39, s56, 3
	s_waitcnt lgkmcnt(0)
	v_readlane_b32 s48, v250, s39
	s_lshl_b32 s30, s48, 10
	s_and_b32 s30, s30, 0x3fffc00
	v_lshl_add_u64 v[2:3], v[226:227], 0, s[30:31]
	s_bfe_u32 s30, s48, 0x100010
	s_lshl_b32 s30, s30, 10
	v_lshl_add_u64 v[72:73], v[226:227], 0, s[30:31]
	s_or_b32 s30, s39, 1
	v_readlane_b32 s48, v250, s30
	s_lshl_b32 s30, s48, 10
	s_and_b32 s30, s30, 0x3fffc00
	global_load_dwordx4 v[68:71], v[2:3], off
	s_nop 0
	global_load_dwordx4 v[72:75], v[72:73], off
	v_lshl_add_u64 v[2:3], v[226:227], 0, s[30:31]
	s_bfe_u32 s30, s48, 0x100010
	s_lshl_b32 s30, s30, 10
	v_lshl_add_u64 v[80:81], v[226:227], 0, s[30:31]
	s_or_b32 s30, s39, 2
	v_readlane_b32 s48, v250, s30
	s_lshl_b32 s30, s48, 10
	s_and_b32 s30, s30, 0x3fffc00
	global_load_dwordx4 v[76:79], v[2:3], off
	s_nop 0
	global_load_dwordx4 v[80:83], v[80:81], off
	v_lshl_add_u64 v[2:3], v[226:227], 0, s[30:31]
	s_bfe_u32 s30, s48, 0x100010
	s_lshl_b32 s30, s30, 10
	v_lshl_add_u64 v[88:89], v[226:227], 0, s[30:31]
	s_or_b32 s30, s39, 3
	v_readlane_b32 s48, v250, s30
	s_lshl_b32 s30, s48, 10
	s_and_b32 s30, s30, 0x3fffc00
	global_load_dwordx4 v[84:87], v[2:3], off
	s_nop 0
	global_load_dwordx4 v[88:91], v[88:89], off
	v_lshl_add_u64 v[2:3], v[226:227], 0, s[30:31]
	s_bfe_u32 s30, s48, 0x100010
	s_lshl_b32 s30, s30, 10
	v_lshl_add_u64 v[96:97], v[226:227], 0, s[30:31]
	s_or_b32 s30, s39, 4
	v_readlane_b32 s48, v250, s30
	s_lshl_b32 s30, s48, 10
	s_and_b32 s30, s30, 0x3fffc00
	global_load_dwordx4 v[92:95], v[2:3], off
	s_nop 0
	global_load_dwordx4 v[96:99], v[96:97], off
	v_lshl_add_u64 v[2:3], v[226:227], 0, s[30:31]
	s_bfe_u32 s30, s48, 0x100010
	s_lshl_b32 s30, s30, 10
	v_lshl_add_u64 v[104:105], v[226:227], 0, s[30:31]
	s_or_b32 s30, s39, 5
	v_readlane_b32 s48, v250, s30
	s_lshl_b32 s30, s48, 10
	s_and_b32 s30, s30, 0x3fffc00
	global_load_dwordx4 v[100:103], v[2:3], off
	s_nop 0
	global_load_dwordx4 v[104:107], v[104:105], off
	v_lshl_add_u64 v[2:3], v[226:227], 0, s[30:31]
	s_bfe_u32 s30, s48, 0x100010
	s_lshl_b32 s30, s30, 10
	v_lshl_add_u64 v[112:113], v[226:227], 0, s[30:31]
	s_or_b32 s30, s39, 6
	v_readlane_b32 s48, v250, s30
	s_lshl_b32 s30, s48, 10
	s_and_b32 s30, s30, 0x3fffc00
	global_load_dwordx4 v[108:111], v[2:3], off
	s_nop 0
	global_load_dwordx4 v[112:115], v[112:113], off
	v_lshl_add_u64 v[2:3], v[226:227], 0, s[30:31]
	s_bfe_u32 s30, s48, 0x100010
	s_lshl_b32 s30, s30, 10
	v_lshl_add_u64 v[124:125], v[226:227], 0, s[30:31]
	s_or_b32 s30, s39, 7
	v_readlane_b32 s39, v250, s30
	s_lshl_b32 s30, s39, 10
	s_and_b32 s30, s30, 0x3fffc00
	global_load_dwordx4 v[120:123], v[2:3], off
	s_nop 0
	global_load_dwordx4 v[124:127], v[124:125], off
	v_lshl_add_u64 v[2:3], v[226:227], 0, s[30:31]
	s_bfe_u32 s30, s39, 0x100010
	s_lshl_b32 s30, s30, 10
	v_lshl_add_u64 v[148:149], v[226:227], 0, s[30:31]
	global_load_dwordx4 v[144:147], v[2:3], off
	s_nop 0
	global_load_dwordx4 v[148:151], v[148:149], off
	s_waitcnt vmcnt(16)
	s_branch .Lpv_go2
.LBB0_1823:
	s_waitcnt vmcnt(0)
.Lpv_go2:
	s_and_b32 s30, s38, 0xff
	s_add_i32 s30, s30, 15
	s_and_b32 s30, s30, 0x1f0
	s_min_u32 s48, s30, 0x80
	s_bfe_u32 s30, s38, 0x80008
	s_add_i32 s30, s30, 15
	s_and_b32 s30, s30, 0x1f0
	s_min_u32 s60, s30, 0x80
	s_bfe_u32 s30, s38, 0x80010
	s_add_i32 s30, s30, 15
	s_and_b32 s30, s30, 0x1f0
	s_min_u32 s61, s30, 0x80
	s_and_b64 s[38:39], s[6:7], exec
	s_cselect_b32 s30, s60, s61
	s_and_b64 s[38:39], s[40:41], exec
	s_cselect_b32 s30, s48, s30
	s_and_b64 s[38:39], s[42:43], exec
	s_cselect_b32 s30, 0, s30
	s_lshr_b32 s38, s30, 4
	s_min_u32 s70, s38, 7
	s_cmp_lg_u32 s59, s70
	s_cbranch_scc1 .LBB0_1832
	s_ashr_i32 s38, s57, 31
	s_add_u32 s52, s0, s57
	s_addc_u32 s53, s1, s38
	s_lshl_b64 s[38:39], s[52:53], 12
	v_cndmask_b32_e64 v1, 0, 1, s[44:45]
	v_lshl_add_u64 v[2:3], v[232:233], 0, s[38:39]
	v_cmp_ne_u32_e64 s[38:39], 1, v1
	s_andn2_b64 vcc, exec, s[44:45]
	s_cbranch_vccnz .LBB0_1833
	global_load_dwordx4 v[128:131], v[2:3], off
	s_and_b64 vcc, exec, s[38:39]
	s_cbranch_vccz .LBB0_1834
